# nt cache policy also on the rwkv post pass loads (T4) and the f32 expert weight loads of the bf16 weight copy (T3b)
# baseline (speedup 1.0000x reference)
; __device__ __forceinline__ void moe_weights_ph(const int WID_, const float* __restrict__ wg, const float* __restrict__ wu, const float* __restrict__ wd, bf16* __restrict__ wgu_t, bf16* __restrict__ wd_t, char* lds, int vb, int nvb, const float* __restrict__ nw3) {
;     ...
;     const int kq = lane >> 3, nq = lane & 7, c = lane & 7;
;     const float* sp; int ldw; bf16* dp; int ldt; const float* ksp;
;     ...
;     float4 vn[8];
;     int it = vb * 8 + wv;
;     MW_DECODE(it);
; #pragma unroll
;     for (int i = 0; i < 8; ++i) vn[i] = *(const float4*)(sp + (size_t)(8 * i + kq) * ldw + 4 * nq);
.LBB0_1760:
	s_or_b64 exec, exec, s[0:1]
	s_movk_i32 s0, 0x6000
	v_cmp_gt_i32_e32 vcc, s0, v47
	s_and_saveexec_b64 s[0:1], vcc
	s_cbranch_execz .LBB0_1769
	v_bfe_u32 v54, v7, 3, 3
	v_or_b32_e32 v61, 56, v54
	v_or_b32_e32 v60, 48, v54
	v_and_b32_e32 v7, 7, v7
	v_mul_u32_u24_e32 v1, v0, v61
	v_mov_b32_e32 v43, 0
	v_lshlrev_b32_e32 v42, 4, v7
	v_lshlrev_b32_e32 v4, 2, v1
	v_mul_u32_u24_e32 v1, v0, v60
	v_or_b32_e32 v59, 40, v54
	v_lshl_add_u64 v[2:3], v[2:3], 0, v[42:43]
	v_mov_b32_e32 v5, v43
	v_lshlrev_b32_e32 v8, 2, v1
	v_mov_b32_e32 v9, v43
	v_or_b32_e32 v58, 32, v54
	v_lshl_add_u64 v[4:5], v[2:3], 0, v[4:5]
	v_lshl_add_u64 v[12:13], v[2:3], 0, v[8:9]
	v_mul_u32_u24_e32 v1, v0, v59
	global_load_dwordx4 v[8:11], v[4:5], off nt
	s_nop 0
	global_load_dwordx4 v[12:15], v[12:13], off nt
	v_lshlrev_b32_e32 v4, 2, v1
	v_mul_u32_u24_e32 v1, v0, v58
	v_or_b32_e32 v57, 24, v54
	v_mov_b32_e32 v5, v43
	v_lshlrev_b32_e32 v16, 2, v1
	v_mov_b32_e32 v17, v43
	v_or_b32_e32 v56, 16, v54
	v_lshl_add_u64 v[4:5], v[2:3], 0, v[4:5]
	v_lshl_add_u64 v[20:21], v[2:3], 0, v[16:17]
	v_mul_u32_u24_e32 v1, v0, v57
	global_load_dwordx4 v[16:19], v[4:5], off nt
	s_nop 0
	global_load_dwordx4 v[20:23], v[20:21], off nt
	v_lshlrev_b32_e32 v4, 2, v1
	v_mul_u32_u24_e32 v1, v0, v56
	v_or_b32_e32 v55, 8, v54
	v_mov_b32_e32 v5, v43
	v_lshlrev_b32_e32 v24, 2, v1
	v_mov_b32_e32 v25, v43
	v_lshl_add_u64 v[4:5], v[2:3], 0, v[4:5]
	v_lshl_add_u64 v[28:29], v[2:3], 0, v[24:25]
	v_mul_u32_u24_e32 v1, v0, v55
	global_load_dwordx4 v[24:27], v[4:5], off nt
	s_nop 0
	global_load_dwordx4 v[28:31], v[28:29], off nt
	v_lshlrev_b32_e32 v4, 2, v1
	v_mov_b32_e32 v5, v43
	v_mul_u32_u24_e32 v0, v0, v54
	v_lshl_add_u64 v[4:5], v[2:3], 0, v[4:5]
	v_lshlrev_b32_e32 v0, 2, v0
	v_mov_b32_e32 v1, v43
	v_lshl_add_u64 v[0:1], v[2:3], 0, v[0:1]
	global_load_dwordx4 v[32:35], v[4:5], off nt
	global_load_dwordx4 v[36:39], v[0:1], off nt
	v_lshl_add_u32 v1, v6, 14, 0
	v_mul_u32_u24_e32 v3, 0x420, v7
	v_lshlrev_b32_e32 v4, 2, v54
	v_lshlrev_b32_e32 v0, 2, v7
	v_add_u32_e32 v2, v1, v42
	v_add3_u32 v62, v1, v3, v4
	v_mul_u32_u24_e32 v1, 0x84, v54
	v_lshlrev_b32_e32 v46, 3, v7
	s_lshl_b32 s8, s94, 3
	s_mov_b64 s[2:3], 0
	v_add_u32_e32 v63, v2, v1
	s_mov_b32 s9, 0x2aaaaaab
	s_movk_i32 s12, 0x1ff
	v_lshlrev_b32_e32 v42, 2, v0
	v_mov_b32_e32 v64, 13
	v_mov_b32_e32 v65, 2
	v_mov_b32_e32 v66, 5
	v_mov_b32_e32 v67, 8
	v_mov_b32_e32 v68, 6
	s_branch .LBB0_1763
; __device__ __forceinline__ unsigned pk2(float lo, float hi) { const f32x2h v = {lo, hi}; const bf16x2h b = __builtin_convertvector(v, bf16x2h); return __builtin_bit_cast(unsigned, b); }
; __device__ __forceinline__ void moe_weights_ph(const int WID_, const float* __restrict__ wg, const float* __restrict__ wu, const float* __restrict__ wd, bf16* __restrict__ wgu_t, bf16* __restrict__ wd_t, char* lds, int vb, int nvb, const float* __restrict__ nw3) {
;     ...
;     for (; it < NIT; it += nvb * 8) {
;         bf16* dcur = dp; const int ldtc = ldt; const float* kcur = ksp;
;         float4 ks0 = make_float4(1.f, 1.f, 1.f, 1.f), ks1 = ks0;
;         if (kcur) { ks0 = *(const float4*)(kcur + 8 * c); ks1 = *(const float4*)(kcur + 8 * c + 4); }
; #pragma unroll
;         for (int i = 0; i < 8; ++i) { float* d = scr + (8 * i + kq) * 33 + 4 * nq; d[0] = vn[i].x; d[1] = vn[i].y; d[2] = vn[i].z; d[3] = vn[i].w; }
;         MW_DECODE(it + nvb * 8);
; #pragma unroll
;         for (int i = 0; i < 8; ++i) vn[i] = *(const float4*)(sp + (size_t)(8 * i + kq) * ldw + 4 * nq);
;         __builtin_amdgcn_s_waitcnt(0xc07f); asm volatile("" ::: "memory");
; #pragma unroll
;         for (int j = 0; j < 4; ++j) { const int n = (lane >> 3) + 8 * j; const float* s = scr + (8 * c) * 33 + n;
;             uint4 o; o.x = pk2(s[0 * 33] * ks0.x, s[1 * 33] * ks0.y); o.y = pk2(s[2 * 33] * ks0.z, s[3 * 33] * ks0.w); o.z = pk2(s[4 * 33] * ks1.x, s[5 * 33] * ks1.y); o.w = pk2(s[6 * 33] * ks1.z, s[7 * 33] * ks1.w);
;             *(uint4*)(dcur + (size_t)n * ldtc + 8 * c) = o; }
;         __builtin_amdgcn_s_waitcnt(0xc07f); asm volatile("" ::: "memory");
.LBB0_1762:
	s_or_b64 exec, exec, s[4:5]
	v_mul_u32_u24_e32 v9, v8, v54
	v_lshl_add_u64 v[10:11], v[12:13], 0, v[42:43]
	v_lshlrev_b32_e32 v12, 2, v9
	v_mov_b32_e32 v13, v43
	v_mul_u32_u24_e32 v9, v8, v55
	v_lshl_add_u64 v[12:13], v[10:11], 0, v[12:13]
	v_lshlrev_b32_e32 v14, 2, v9
	v_mov_b32_e32 v15, v43
	v_mul_u32_u24_e32 v9, v8, v56
	v_lshl_add_u64 v[14:15], v[10:11], 0, v[14:15]
	global_load_dwordx4 v[36:39], v[12:13], off nt
	global_load_dwordx4 v[32:35], v[14:15], off nt
	v_lshlrev_b32_e32 v12, 2, v9
	v_mov_b32_e32 v13, v43
	v_mul_u32_u24_e32 v9, v8, v57
	v_lshl_add_u64 v[12:13], v[10:11], 0, v[12:13]
	v_lshlrev_b32_e32 v14, 2, v9
	v_mov_b32_e32 v15, v43
	v_mul_u32_u24_e32 v9, v8, v58
	v_lshl_add_u64 v[14:15], v[10:11], 0, v[14:15]
	global_load_dwordx4 v[28:31], v[12:13], off nt
	global_load_dwordx4 v[24:27], v[14:15], off nt
	v_lshlrev_b32_e32 v12, 2, v9
	v_mov_b32_e32 v13, v43
	v_mul_u32_u24_e32 v9, v8, v59
	v_lshl_add_u64 v[12:13], v[10:11], 0, v[12:13]
	v_lshlrev_b32_e32 v14, 2, v9
	v_mov_b32_e32 v15, v43
	v_mul_u32_u24_e32 v9, v8, v60
	v_mul_u32_u24_e32 v8, v8, v61
	v_lshl_add_u64 v[14:15], v[10:11], 0, v[14:15]
	global_load_dwordx4 v[20:23], v[12:13], off nt
	global_load_dwordx4 v[16:19], v[14:15], off nt
	v_lshlrev_b32_e32 v12, 2, v9
	v_mov_b32_e32 v13, v43
	v_lshlrev_b32_e32 v8, 2, v8
	v_mov_b32_e32 v9, v43
	v_lshl_add_u64 v[12:13], v[10:11], 0, v[12:13]
	v_lshl_add_u64 v[8:9], v[10:11], 0, v[8:9]
	global_load_dwordx4 v[12:15], v[12:13], off nt
	s_nop 0
	global_load_dwordx4 v[8:11], v[8:9], off nt
	s_waitcnt lgkmcnt(0)
	ds_read2_b32 v[74:75], v62 offset1:8
	ds_read2_b32 v[76:77], v62 offset0:33 offset1:41
	ds_read2_b32 v[78:79], v62 offset0:66 offset1:74
	ds_read2_b32 v[80:81], v62 offset0:99 offset1:107
	ds_read2_b32 v[82:83], v62 offset0:132 offset1:140
	ds_read2_b32 v[84:85], v62 offset0:165 offset1:173
	ds_read2_b32 v[86:87], v62 offset0:198 offset1:206
	ds_read2_b32 v[88:89], v62 offset0:231 offset1:239
	v_lshlrev_b32_e32 v70, 1, v46
	v_mov_b32_e32 v71, v43
	v_lshl_add_u64 v[44:45], v[44:45], 0, v[70:71]
	s_waitcnt lgkmcnt(7)
	v_mov_b32_e32 v70, v74
	s_waitcnt lgkmcnt(6)
	v_mov_b32_e32 v71, v76
	s_waitcnt lgkmcnt(5)
	v_mov_b32_e32 v72, v78
	s_waitcnt lgkmcnt(4)
	v_mov_b32_e32 v73, v80
	v_pk_mul_f32 v[70:71], v[4:5], v[70:71]
	v_pk_mul_f32 v[72:73], v[6:7], v[72:73]
	v_cvt_pk_bf16_f32 v70, v70, v71
	v_cvt_pk_bf16_f32 v71, v72, v73
	s_waitcnt lgkmcnt(3)
	v_mov_b32_e32 v72, v82
	s_waitcnt lgkmcnt(2)
	v_mov_b32_e32 v73, v84
	s_waitcnt lgkmcnt(1)
	v_mov_b32_e32 v90, v86
	s_waitcnt lgkmcnt(0)
	v_mov_b32_e32 v91, v88
	v_pk_mul_f32 v[72:73], v[0:1], v[72:73]
	v_pk_mul_f32 v[90:91], v[2:3], v[90:91]
	v_cvt_pk_bf16_f32 v72, v72, v73
	v_cvt_pk_bf16_f32 v73, v90, v91
	v_mul_hi_i32_i24_e32 v91, v40, v54
	v_mul_i32_i24_e32 v90, v40, v54
	v_lshl_add_u64 v[90:91], v[90:91], 1, v[44:45]
	v_mov_b32_e32 v76, v75
	v_mov_b32_e32 v80, v79
	global_store_dwordx4 v[90:91], v[70:73], off
	v_mov_b32_e32 v84, v83
	v_mov_b32_e32 v88, v87
	v_pk_mul_f32 v[70:71], v[4:5], v[76:77]
	v_pk_mul_f32 v[72:73], v[6:7], v[80:81]
	v_cvt_pk_bf16_f32 v70, v70, v71
	v_cvt_pk_bf16_f32 v71, v72, v73
	v_pk_mul_f32 v[72:73], v[0:1], v[84:85]
	v_pk_mul_f32 v[74:75], v[2:3], v[88:89]
	v_cvt_pk_bf16_f32 v72, v72, v73
	v_cvt_pk_bf16_f32 v73, v74, v75
	v_mul_hi_i32_i24_e32 v75, v40, v55
	v_mul_i32_i24_e32 v74, v40, v55
	v_lshl_add_u64 v[74:75], v[74:75], 1, v[44:45]
	ds_read2_b32 v[76:77], v62 offset0:16 offset1:24
	ds_read2_b32 v[78:79], v62 offset0:49 offset1:57
	global_store_dwordx4 v[74:75], v[70:73], off
	ds_read2_b32 v[74:75], v62 offset0:82 offset1:90
	ds_read2_b32 v[80:81], v62 offset0:115 offset1:123
	ds_read2_b32 v[82:83], v62 offset0:148 offset1:156
	ds_read2_b32 v[84:85], v62 offset0:181 offset1:189
	ds_read2_b32 v[86:87], v62 offset0:214 offset1:222
	ds_read2_b32 v[88:89], v62 offset0:247 offset1:255
	s_waitcnt lgkmcnt(7)
	v_mov_b32_e32 v70, v76
	s_waitcnt lgkmcnt(6)
	v_mov_b32_e32 v71, v78
	s_waitcnt lgkmcnt(5)
	v_mov_b32_e32 v72, v74
	s_waitcnt lgkmcnt(4)
	v_mov_b32_e32 v73, v80
	v_pk_mul_f32 v[70:71], v[4:5], v[70:71]
	v_pk_mul_f32 v[72:73], v[6:7], v[72:73]
	v_cvt_pk_bf16_f32 v70, v70, v71
	v_cvt_pk_bf16_f32 v71, v72, v73
	s_waitcnt lgkmcnt(3)
	v_mov_b32_e32 v72, v82
	s_waitcnt lgkmcnt(2)
	v_mov_b32_e32 v73, v84
	v_mov_b32_e32 v78, v77
	v_mov_b32_e32 v80, v75
	v_mov_b32_e32 v84, v83
	v_pk_mul_f32 v[72:73], v[0:1], v[72:73]
	s_waitcnt lgkmcnt(1)
	v_mov_b32_e32 v90, v86
	s_waitcnt lgkmcnt(0)
	v_mov_b32_e32 v91, v88
	v_pk_mul_f32 v[4:5], v[4:5], v[78:79]
	v_pk_mul_f32 v[6:7], v[6:7], v[80:81]
	v_pk_mul_f32 v[0:1], v[0:1], v[84:85]
	v_mov_b32_e32 v88, v87
	v_pk_mul_f32 v[90:91], v[2:3], v[90:91]
	v_cvt_pk_bf16_f32 v4, v4, v5
	v_cvt_pk_bf16_f32 v5, v6, v7
	v_cvt_pk_bf16_f32 v6, v0, v1
	v_pk_mul_f32 v[0:1], v[2:3], v[88:89]
	v_cvt_pk_bf16_f32 v72, v72, v73
	v_cvt_pk_bf16_f32 v73, v90, v91
	v_mul_hi_i32_i24_e32 v91, v40, v56
	v_mul_i32_i24_e32 v90, v40, v56
	v_cvt_pk_bf16_f32 v7, v0, v1
	v_mul_hi_i32_i24_e32 v1, v40, v57
	v_mul_i32_i24_e32 v0, v40, v57
	v_lshl_add_u64 v[90:91], v[90:91], 1, v[44:45]
	v_lshl_add_u64 v[0:1], v[0:1], 1, v[44:45]
	global_store_dwordx4 v[90:91], v[70:73], off
	global_store_dwordx4 v[0:1], v[4:7], off
	s_waitcnt lgkmcnt(0)
	s_movk_i32 s4, 0x5fff
	v_cmp_lt_i32_e32 vcc, s4, v47
	s_or_b64 s[2:3], vcc, s[2:3]
	v_mov_b64_e32 v[44:45], v[50:51]
	v_mov_b64_e32 v[40:41], v[52:53]
	s_andn2_b64 exec, exec, s[2:3]
	s_cbranch_execz .LBB0_1769
.LBB0_1763:
	v_cmp_ne_u64_e32 vcc, 0, v[48:49]
	v_mov_b32_e32 v2, 1.0
	v_mov_b32_e32 v3, 1.0
	v_mov_b32_e32 v0, 1.0
	v_mov_b32_e32 v1, 1.0
	v_mov_b32_e32 v6, 1.0
	v_mov_b32_e32 v7, 1.0
	v_mov_b32_e32 v4, 1.0
	v_mov_b32_e32 v5, 1.0
	s_and_saveexec_b64 s[4:5], vcc
	s_cbranch_execz .LBB0_1765
	v_lshlrev_b32_e32 v0, 2, v46
	v_mov_b32_e32 v1, v43
	v_lshl_add_u64 v[4:5], v[48:49], 0, v[0:1]
	global_load_dwordx4 v[0:3], v[4:5], off offset:16 nt
	s_nop 0
	global_load_dwordx4 v[4:7], v[4:5], off nt

; __device__ __forceinline__ int lane_id() { int l; asm volatile("v_mbcnt_lo_u32_b32 %0, -1, 0\n\tv_mbcnt_hi_u32_b32 %0, -1, %0" : "=v"(l)); return l; }
; __device__ __forceinline__ void rwkv_post_ph(const int WID_, const float* __restrict__ Y, const float* __restrict__ RK, const bf16* __restrict__ proj, const float* __restrict__ mu, const bf16* __restrict__ G, ...
;     const int lane = lane_id(), tk = WID_, grp = lane, ch0 = grp * 8, head = grp >> 3;
;     const float4 mv0 = *(const float4*)(mu + 1024 + ch0), mv1 = *(const float4*)(mu + 1024 + ch0 + 4), lw0 = *(const float4*)(lnw + ch0), lw1 = *(const float4*)(lnw + ch0 + 4), lb0 = *(const float4*)(lnb + ch0), lb1 = *(const float4*)(lnb + ch0 + 4);
;     const float muv[8] = {mv0.x, mv0.y, mv0.z, mv0.w, mv1.x, mv1.y, mv1.z, mv1.w}, lw_[8] = {lw0.x, lw0.y, lw0.z, lw0.w, lw1.x, lw1.y, lw1.z, lw1.w}, lb_[8] = {lb0.x, lb0.y, lb0.z, lb0.w, lb1.x, lb1.y, lb1.z, lb1.w};
;     const int g_lo = (GB * (M / 16)) / GN, g_hi = ((GB + 1) * (M / 16)) / GN;
;     for (int g = g_lo; g < g_hi; ++g) { const int m0 = g * 16 + tk;
;         float4 ya[2], yb[2]; uint4 vv[2], pv[2], gg[2]; float rk[2];
; #pragma unroll
;         for (int u = 0; u < 2; ++u) { const int m = m0 + 8 * u;
;             ya[u] = *(const float4*)(Y + (size_t)m * 512 + ch0); yb[u] = *(const float4*)(Y + (size_t)m * 512 + ch0 + 4);
;             vv[u] = *(const uint4*)(proj + (size_t)m * DSHIFT + 1024 + ch0);
;             pv[u] = (m & (S - 1)) ? *(const uint4*)(proj + (size_t)(m - 1) * DSHIFT + 1024 + ch0) : make_uint4(0, 0, 0, 0);
;             gg[u] = *(const uint4*)(G + (size_t)m * 512 + ch0); rk[u] = RK[(size_t)m * 8 + head]; }
; #pragma unroll
;         for (int u = 0; u < 2; ++u) {
;             const float y[8] = {ya[u].x, ya[u].y, ya[u].z, ya[u].w, yb[u].x, yb[u].y, yb[u].z, yb[u].w};
;             float s = 0.f;
; #pragma unroll
;             for (int e = 0; e < 8; ++e) s += y[e];
;             s += dpp16<0xB1>(s); s += dpp16<0x4E>(s); s += dpp16<0x141>(s);
;             const float mean = s * (1.f / 64.f); float q = 0.f;
; #pragma unroll
;             for (int e = 0; e < 8; ++e) { const float d = y[e] - mean; q += d * d; }
;             q += dpp16<0xB1>(q); q += dpp16<0x4E>(q); q += dpp16<0x141>(q);
;             const float rstd = rsqrtf(q * (1.f / 64.f) + 64e-5f);
.LBB0_1869:
	s_or_b64 exec, exec, s[0:1]
	s_add_u32 s4, s92, 0x34000000
	s_addc_u32 s5, s93, 0
	s_add_u32 s12, s92, 0x38000000
	s_addc_u32 s13, s93, 0
	s_bitcmp0_b32 s87, 3
	s_cselect_b64 s[18:19], -1, 0
	s_and_b64 vcc, exec, s[18:19]
	s_waitcnt lgkmcnt(0)
	s_barrier
	s_cbranch_vccnz .LBB0_1879
	s_lshl_b32 s2, s87, 12
	s_abs_i32 s1, s2
	v_readlane_b32 s22, v242, 32
	s_mul_hi_u32 s3, s1, s22
	v_readlane_b32 s33, v242, 33
	s_mul_i32 s8, s3, s33
	s_bfe_i32 s0, s87, 0x10013
	v_readlane_b32 s23, v243, 45
	s_sub_i32 s1, s1, s8
	s_xor_b32 s0, s0, s23
	s_add_i32 s8, s3, 1
	s_sub_i32 s9, s1, s33
	s_cmp_ge_u32 s1, s33
	s_cselect_b32 s3, s8, s3
	s_cselect_b32 s1, s9, s1
	s_add_i32 s8, s3, 1
	s_cmp_ge_u32 s1, s33
	s_cselect_b32 s1, s8, s3
	s_add_i32 s8, s2, 0x1000
	s_xor_b32 s2, s2, 0xfffff000
	s_max_i32 s2, s8, s2
	s_ashr_i32 s9, s8, 31
	s_mul_hi_u32 s8, s2, s22
	s_mul_i32 s22, s8, s33
	s_xor_b32 s1, s1, s0
	s_sub_i32 s2, s2, s22
	s_sub_i32 s3, s1, s0
	s_xor_b32 s9, s9, s23
	s_add_i32 s22, s8, 1
	s_sub_i32 s23, s2, s33
	s_cmp_ge_u32 s2, s33
	s_cselect_b32 s8, s22, s8
	s_cselect_b32 s2, s23, s2
	s_add_i32 s22, s8, 1
	s_cmp_ge_u32 s2, s33
	s_cselect_b32 s2, s22, s8
	s_xor_b32 s2, s2, s9
	s_sub_i32 s8, s2, s9
	s_cmp_ge_i32 s3, s8
	v_mbcnt_lo_u32_b32 v24, -1, 0
	v_mbcnt_hi_u32_b32 v24, -1, v24
	s_cbranch_scc1 .LBB0_1879
	v_lshlrev_b32_e32 v26, 3, v24
	v_ashrrev_i32_e32 v27, 31, v26
	v_lshlrev_b64 v[28:29], 2, v[26:27]
	v_lshl_add_u64 v[0:1], s[64:65], 0, v[28:29]
	s_mov_b64 s[22:23], 0x1000
	v_readlane_b32 s36, v243, 6
	v_lshl_add_u64 v[4:5], v[0:1], 0, s[22:23]
	v_readlane_b32 s46, v243, 16
	v_readlane_b32 s47, v243, 17
	v_readlane_b32 s48, v243, 18
	v_readlane_b32 s49, v243, 19
	v_add_co_u32_e32 v0, vcc, 0x1000, v0
	v_lshl_add_u64 v[12:13], s[46:47], 0, v[28:29]
	v_lshl_add_u64 v[20:21], s[48:49], 0, v[28:29]
	v_addc_co_u32_e32 v1, vcc, 0, v1, vcc
	global_load_dwordx4 v[0:3], v[0:1], off nt
	s_nop 0
	global_load_dwordx4 v[4:7], v[4:5], off offset:16 nt
	s_nop 0
	global_load_dwordx4 v[8:11], v[12:13], off offset:16 nt
	s_nop 0
	global_load_dwordx4 v[12:15], v[12:13], off nt
	s_nop 0
	global_load_dwordx4 v[16:19], v[20:21], off offset:16 nt
	s_nop 0
	global_load_dwordx4 v[20:23], v[20:21], off nt
	v_ashrrev_i32_e32 v24, 3, v24
	s_lshl_b32 s1, s1, 4
	v_readlane_b32 s2, v243, 44
	v_lshlrev_b64 v[26:27], 1, v[26:27]
	v_ashrrev_i32_e32 v25, 31, v24
	s_add_i32 s1, s2, s1
	s_lshl_b32 s0, s0, 4
	v_lshl_add_u64 v[60:61], s[12:13], 0, v[28:29]
	v_lshl_add_u64 v[62:63], s[4:5], 0, v[26:27]
	v_lshl_add_u64 v[64:65], v[24:25], 2, s[10:11]
	v_lshl_add_u64 v[66:67], s[26:27], 0, v[26:27]
	v_lshl_add_u64 v[68:69], s[92:93], 0, v[26:27]
	s_sub_i32 s0, s1, s0
	s_mov_b32 s2, 0x3c800000
	s_mov_b32 s9, 0x800000
	v_mov_b32_e32 v71, 0xe00
	v_mov_b32_e32 v70, 0x3a27c5ac
	v_readlane_b32 s37, v243, 7
	v_readlane_b32 s38, v243, 8
	v_readlane_b32 s39, v243, 9
	v_readlane_b32 s40, v243, 10
	v_readlane_b32 s41, v243, 11
	v_readlane_b32 s42, v243, 12
	v_readlane_b32 s43, v243, 13
	v_readlane_b32 s44, v243, 14
	v_readlane_b32 s45, v243, 15
	v_readlane_b32 s50, v243, 20
	v_readlane_b32 s51, v243, 21
	s_branch .LBB0_1874
.LBB0_1872:
	s_add_i32 s1, s0, 7
	v_mad_i64_i32 v[24:25], s[34:35], s1, v71, v[68:69]
	global_load_dwordx4 v[24:27], v[24:25], off offset:2048 nt
.LBB0_1873:
	s_lshl_b64 s[38:39], s[38:39], 5
	v_lshl_add_u64 v[74:75], s[40:41], 1, v[62:63]
	v_lshl_add_u64 v[96:97], v[64:65], 0, s[38:39]
	global_load_dwordx4 v[74:77], v[74:75], off nt
	s_waitcnt vmcnt(1)
	v_lshlrev_b32_e32 v94, 16, v46
	v_and_b32_e32 v95, 0xffff0000, v46
	global_load_dword v46, v[96:97], off
	v_add_f32_e32 v73, 0, v28
	v_lshlrev_b32_e32 v84, 16, v50
	v_lshlrev_b32_e32 v86, 16, v54
	v_and_b32_e32 v85, 0xffff0000, v50
	v_and_b32_e32 v87, 0xffff0000, v54
	v_lshlrev_b32_e32 v50, 16, v51
	v_lshlrev_b32_e32 v54, 16, v55
	v_and_b32_e32 v51, 0xffff0000, v51
	v_and_b32_e32 v55, 0xffff0000, v55
	v_add_f32_e32 v98, 0, v36
	v_add_f32_e32 v73, v73, v29
	v_pk_add_f32 v[54:55], v[54:55], v[50:51] neg_lo:[0,1] neg_hi:[0,1]
	v_add_f32_e32 v98, v98, v37
	v_add_f32_e32 v73, v73, v30
	v_pk_fma_f32 v[50:51], v[6:7], v[54:55], v[50:51]
	v_add_f32_e32 v54, v98, v38
	v_add_f32_e32 v55, v73, v31
	v_add_f32_e32 v54, v54, v39
	v_add_f32_e32 v55, v55, v32
	v_add_f32_e32 v54, v54, v40
	v_add_f32_e32 v55, v55, v33
	v_add_f32_e32 v54, v54, v41
	v_add_f32_e32 v55, v55, v34
	v_add_f32_e32 v54, v54, v42
	v_add_f32_e32 v55, v55, v35
	v_add_f32_e32 v54, v54, v43
	v_lshlrev_b32_e32 v78, 16, v48
	v_add_f32_dpp v55, v55, v55 quad_perm:[1,0,3,2] row_mask:0xf bank_mask:0xf bound_ctrl:1
	v_add_f32_dpp v54, v54, v54 quad_perm:[1,0,3,2] row_mask:0xf bank_mask:0xf bound_ctrl:1
	v_lshlrev_b32_e32 v80, 16, v52
	v_and_b32_e32 v79, 0xffff0000, v48
	v_and_b32_e32 v81, 0xffff0000, v52
	v_lshlrev_b32_e32 v48, 16, v49
	v_lshlrev_b32_e32 v52, 16, v53
	v_and_b32_e32 v49, 0xffff0000, v49
	v_and_b32_e32 v53, 0xffff0000, v53
	v_add_f32_dpp v55, v55, v55 quad_perm:[2,3,0,1] row_mask:0xf bank_mask:0xf bound_ctrl:1
	v_add_f32_dpp v54, v54, v54 quad_perm:[2,3,0,1] row_mask:0xf bank_mask:0xf bound_ctrl:1
	v_pk_add_f32 v[52:53], v[52:53], v[48:49] neg_lo:[0,1] neg_hi:[0,1]
	v_pk_add_f32 v[80:81], v[80:81], v[78:79] neg_lo:[0,1] neg_hi:[0,1]
	v_add_f32_dpp v55, v55, v55 row_half_mirror row_mask:0xf bank_mask:0xf bound_ctrl:1
	v_add_f32_dpp v73, v54, v54 row_half_mirror row_mask:0xf bank_mask:0xf bound_ctrl:1
	v_pk_fma_f32 v[48:49], v[2:3], v[52:53], v[48:49]
	v_pk_fma_f32 v[52:53], v[0:1], v[80:81], v[78:79]
	v_mul_f32_e32 v54, 0x3c800000, v55
	v_mul_f32_e32 v78, 0x3c800000, v73
	v_lshlrev_b32_e32 v92, 16, v44
	v_and_b32_e32 v93, 0xffff0000, v44
	v_lshlrev_b32_e32 v44, 16, v45
; __device__ __forceinline__ unsigned pk2(float lo, float hi) { const f32x2h v = {lo, hi}; const bf16x2h b = __builtin_convertvector(v, bf16x2h); return __builtin_bit_cast(unsigned, b); }
; template <int CTRL> __device__ __forceinline__ float dpp16(float x) { return __builtin_bit_cast(float, __builtin_amdgcn_update_dpp(0, __builtin_bit_cast(int, x), CTRL, 0xf, 0xf, true)); }
; __device__ __forceinline__ void rwkv_post_ph(const int WID_, const float* __restrict__ Y, const float* __restrict__ RK, const bf16* __restrict__ proj, const float* __restrict__ mu, const bf16* __restrict__ G, ...
;     ...
;         for (int u = 0; u < 2; ++u) {
;             const float y[8] = {ya[u].x, ya[u].y, ya[u].z, ya[u].w, yb[u].x, yb[u].y, yb[u].z, yb[u].w};
;             float s = 0.f;
; #pragma unroll
;             for (int e = 0; e < 8; ++e) s += y[e];
;             s += dpp16<0xB1>(s); s += dpp16<0x4E>(s); s += dpp16<0x141>(s);
;             const float mean = s * (1.f / 64.f); float q = 0.f;
; #pragma unroll
;             for (int e = 0; e < 8; ++e) { const float d = y[e] - mean; q += d * d; }
;             q += dpp16<0xB1>(q); q += dpp16<0x4E>(q); q += dpp16<0x141>(q);
;             const float rstd = rsqrtf(q * (1.f / 64.f) + 64e-5f);
;             const unsigned wv_[4] = {vv[u].x, vv[u].y, vv[u].z, vv[u].w}, wp_[4] = {pv[u].x, pv[u].y, pv[u].z, pv[u].w}, wg_[4] = {gg[u].x, gg[u].y, gg[u].z, gg[u].w};
;             float o[8];
; #pragma unroll
;             for (int e = 0; e < 8; ++e) { const int w_ = e >> 1; const bool hi = e & 1;
;                 auto ex = [&](unsigned x) { return hi ? __builtin_bit_cast(float, x & 0xffff0000u) : __builtin_bit_cast(float, x << 16); };
;                 float v = ex(wv_[w_]); v += (ex(wp_[w_]) - v) * muv[e];
;                 o[e] = ((y[e] - mean) * rstd * lw_[e] + lb_[e] + rk[u] * v) * ex(wg_[w_]); }
;             *(uint4*)(ymix + (size_t)(m0 + 8 * u) * D + ch0) = make_uint4(pk2(o[0], o[1]), pk2(o[2], o[3]), pk2(o[4], o[5]), pk2(o[6], o[7]));
;         }
	v_and_b32_e32 v45, 0xffff0000, v45
	v_pk_add_f32 v[28:29], v[28:29], v[54:55] op_sel_hi:[1,0] neg_lo:[0,1] neg_hi:[0,1]
	v_lshlrev_b32_e32 v108, 16, v26
	v_and_b32_e32 v109, 0xffff0000, v26
	v_lshlrev_b32_e32 v110, 16, v25
	v_and_b32_e32 v111, 0xffff0000, v25
	v_pk_add_f32 v[36:37], v[36:37], v[78:79] op_sel_hi:[1,0] neg_lo:[0,1] neg_hi:[0,1]
	v_pk_add_f32 v[86:87], v[86:87], v[84:85] neg_lo:[0,1] neg_hi:[0,1]
	v_pk_add_f32 v[30:31], v[30:31], v[54:55] op_sel_hi:[1,0] neg_lo:[0,1] neg_hi:[0,1]
	v_pk_mul_f32 v[96:97], v[28:29], v[28:29]
	v_pk_add_f32 v[42:43], v[42:43], v[78:79] op_sel_hi:[1,0] neg_lo:[0,1] neg_hi:[0,1]
	v_pk_add_f32 v[40:41], v[40:41], v[78:79] op_sel_hi:[1,0] neg_lo:[0,1] neg_hi:[0,1]
	v_pk_add_f32 v[108:109], v[108:109], v[94:95] neg_lo:[0,1] neg_hi:[0,1]
	v_pk_add_f32 v[38:39], v[38:39], v[78:79] op_sel_hi:[1,0] neg_lo:[0,1] neg_hi:[0,1]
	v_pk_add_f32 v[110:111], v[110:111], v[44:45] neg_lo:[0,1] neg_hi:[0,1]
	v_pk_mul_f32 v[78:79], v[36:37], v[36:37]
	v_pk_fma_f32 v[84:85], v[4:5], v[86:87], v[84:85]
	v_pk_mul_f32 v[86:87], v[30:31], v[30:31]
	v_pk_fma_f32 v[94:95], v[4:5], v[108:109], v[94:95]
	v_pk_mul_f32 v[108:109], v[38:39], v[38:39]
	v_pk_fma_f32 v[44:45], v[2:3], v[110:111], v[44:45]
	v_mov_b32_e32 v110, v78
	v_mov_b32_e32 v111, v96
	v_mov_b32_e32 v96, v79
	v_pk_add_f32 v[32:33], v[32:33], v[54:55] op_sel_hi:[1,0] neg_lo:[0,1] neg_hi:[0,1]
	v_pk_add_f32 v[78:79], v[110:111], v[96:97]
	v_mov_b32_e32 v110, v108
	v_mov_b32_e32 v111, v86
	v_pk_mul_f32 v[80:81], v[32:33], v[32:33]
	v_pk_mul_f32 v[106:107], v[40:41], v[40:41]
	v_pk_add_f32 v[78:79], v[110:111], v[78:79]
	v_mov_b32_e32 v86, v109
	v_pk_add_f32 v[34:35], v[34:35], v[54:55] op_sel_hi:[1,0] neg_lo:[0,1] neg_hi:[0,1]
	v_pk_add_f32 v[78:79], v[86:87], v[78:79]
	v_mov_b32_e32 v86, v106
	v_mov_b32_e32 v87, v80
	v_pk_mul_f32 v[54:55], v[34:35], v[34:35]
	v_pk_mul_f32 v[104:105], v[42:43], v[42:43]
	v_pk_add_f32 v[78:79], v[86:87], v[78:79]
	v_mov_b32_e32 v80, v107
	v_pk_add_f32 v[78:79], v[80:81], v[78:79]
	v_mov_b32_e32 v80, v104
	v_mov_b32_e32 v81, v54
	v_pk_add_f32 v[78:79], v[80:81], v[78:79]
	v_mov_b32_e32 v54, v105
	v_pk_add_f32 v[54:55], v[54:55], v[78:79]
	v_lshlrev_b32_e32 v102, 16, v47
	v_and_b32_e32 v103, 0xffff0000, v47
	v_mov_b32_dpp v79, v55 quad_perm:[1,0,3,2] row_mask:0xf bank_mask:0xf bound_ctrl:1
	v_mov_b32_dpp v78, v54 quad_perm:[1,0,3,2] row_mask:0xf bank_mask:0xf bound_ctrl:1
	v_pk_add_f32 v[54:55], v[54:55], v[78:79]
	v_lshlrev_b32_e32 v82, 16, v56
	v_and_b32_e32 v83, 0xffff0000, v56
	v_mov_b32_dpp v79, v55 quad_perm:[2,3,0,1] row_mask:0xf bank_mask:0xf bound_ctrl:1
	v_mov_b32_dpp v78, v54 quad_perm:[2,3,0,1] row_mask:0xf bank_mask:0xf bound_ctrl:1
	v_pk_add_f32 v[54:55], v[54:55], v[78:79]
	v_lshlrev_b32_e32 v56, 16, v57
	v_and_b32_e32 v57, 0xffff0000, v57
	v_mov_b32_dpp v79, v55 row_half_mirror row_mask:0xf bank_mask:0xf bound_ctrl:1
	v_mov_b32_dpp v78, v54 row_half_mirror row_mask:0xf bank_mask:0xf bound_ctrl:1
	v_pk_add_f32 v[54:55], v[54:55], v[78:79]
	v_lshlrev_b32_e32 v88, 16, v58
	v_pk_fma_f32 v[54:55], v[54:55], s[2:3], v[70:71] op_sel_hi:[1,0,0]
	v_and_b32_e32 v89, 0xffff0000, v58
	v_mul_f32_e32 v25, 0x4b800000, v55
	v_cmp_gt_f32_e32 vcc, s9, v55
	v_lshlrev_b32_e32 v58, 16, v59
	v_and_b32_e32 v59, 0xffff0000, v59
	v_cndmask_b32_e32 v25, v55, v25, vcc
	v_rsq_f32_e32 v26, v25
	v_lshl_add_u64 v[90:91], v[66:67], 0, s[36:37]
	v_lshlrev_b32_e32 v96, 16, v24
	v_and_b32_e32 v97, 0xffff0000, v24
	v_mul_f32_e32 v47, 0x45800000, v26
	v_cndmask_b32_e32 v26, v26, v47, vcc
	v_pk_mul_f32 v[28:29], v[28:29], v[26:27] op_sel_hi:[1,0]
	v_pk_mul_f32 v[30:31], v[30:31], v[26:27] op_sel_hi:[1,0]
	v_pk_mul_f32 v[32:33], v[32:33], v[26:27] op_sel_hi:[1,0]
	v_pk_mul_f32 v[34:35], v[34:35], v[26:27] op_sel_hi:[1,0]
	v_mul_f32_e32 v26, 0x4b800000, v54
	v_cmp_gt_f32_e32 vcc, s9, v54
	v_pk_fma_f32 v[28:29], v[12:13], v[28:29], v[20:21]
	v_pk_fma_f32 v[30:31], v[14:15], v[30:31], v[22:23]
	v_cndmask_b32_e32 v26, v54, v26, vcc
	v_pk_fma_f32 v[32:33], v[8:9], v[32:33], v[16:17]
	v_pk_fma_f32 v[34:35], v[10:11], v[34:35], v[18:19]
	v_rsq_f32_e32 v26, v26
	v_pk_fma_f32 v[28:29], v[52:53], v[72:73], v[28:29] op_sel_hi:[1,0,1]
	v_pk_fma_f32 v[30:31], v[48:49], v[72:73], v[30:31] op_sel_hi:[1,0,1]
	v_pk_fma_f32 v[32:33], v[84:85], v[72:73], v[32:33] op_sel_hi:[1,0,1]
	v_pk_fma_f32 v[34:35], v[50:51], v[72:73], v[34:35] op_sel_hi:[1,0,1]
	v_pk_mul_f32 v[28:29], v[28:29], v[82:83]
	v_pk_mul_f32 v[30:31], v[30:31], v[56:57]
	v_pk_mul_f32 v[32:33], v[32:33], v[88:89]
	v_pk_mul_f32 v[34:35], v[34:35], v[58:59]
	v_cvt_pk_bf16_f32 v28, v28, v29
	v_cvt_pk_bf16_f32 v29, v30, v31
	v_cvt_pk_bf16_f32 v30, v32, v33
	v_cvt_pk_bf16_f32 v31, v34, v35
	global_store_dwordx4 v[90:91], v[28:31], off
	v_pk_add_f32 v[24:25], v[96:97], v[92:93] neg_lo:[0,1] neg_hi:[0,1]
	v_lshlrev_b32_e32 v32, 16, v27
	v_mul_f32_e32 v28, 0x45800000, v26
	v_cndmask_b32_e32 v26, v26, v28, vcc
	v_pk_mul_f32 v[28:29], v[36:37], v[26:27] op_sel_hi:[1,0]
	v_pk_fma_f32 v[24:25], v[0:1], v[24:25], v[92:93]
	v_pk_fma_f32 v[28:29], v[12:13], v[28:29], v[20:21]
	v_and_b32_e32 v33, 0xffff0000, v27
	s_waitcnt vmcnt(1)
	v_pk_fma_f32 v[24:25], v[24:25], v[46:47], v[28:29] op_sel_hi:[1,0,1]
	v_pk_mul_f32 v[28:29], v[38:39], v[26:27] op_sel_hi:[1,0]
	v_pk_mul_f32 v[30:31], v[40:41], v[26:27] op_sel_hi:[1,0]
	v_pk_add_f32 v[32:33], v[32:33], v[102:103] neg_lo:[0,1] neg_hi:[0,1]
	v_pk_mul_f32 v[26:27], v[42:43], v[26:27] op_sel_hi:[1,0]
	v_pk_fma_f32 v[28:29], v[14:15], v[28:29], v[22:23]
	v_pk_fma_f32 v[30:31], v[8:9], v[30:31], v[16:17]
	v_pk_fma_f32 v[32:33], v[6:7], v[32:33], v[102:103]
	v_pk_fma_f32 v[26:27], v[10:11], v[26:27], v[18:19]
	v_lshlrev_b32_e32 v98, 16, v74
	v_and_b32_e32 v99, 0xffff0000, v74
	v_lshlrev_b32_e32 v74, 16, v75
	v_and_b32_e32 v75, 0xffff0000, v75
	v_lshlrev_b32_e32 v100, 16, v76
	v_and_b32_e32 v101, 0xffff0000, v76
	v_lshlrev_b32_e32 v76, 16, v77
	v_and_b32_e32 v77, 0xffff0000, v77
	v_pk_fma_f32 v[28:29], v[44:45], v[46:47], v[28:29] op_sel_hi:[1,0,1]
	v_pk_fma_f32 v[30:31], v[94:95], v[46:47], v[30:31] op_sel_hi:[1,0,1]
	v_pk_fma_f32 v[26:27], v[32:33], v[46:47], v[26:27] op_sel_hi:[1,0,1]
	v_pk_mul_f32 v[24:25], v[24:25], v[98:99]
	v_pk_mul_f32 v[28:29], v[28:29], v[74:75]
	v_pk_mul_f32 v[30:31], v[30:31], v[100:101]
	v_pk_mul_f32 v[32:33], v[26:27], v[76:77]
	s_add_i32 s3, s3, 1
	s_add_i32 s0, s0, 16
	v_cvt_pk_bf16_f32 v24, v24, v25
	v_cvt_pk_bf16_f32 v25, v28, v29
	v_cvt_pk_bf16_f32 v26, v30, v31
	v_cvt_pk_bf16_f32 v27, v32, v33
	v_lshl_add_u64 v[28:29], v[66:67], 0, s[22:23]
	s_cmp_lt_i32 s3, s8
	global_store_dwordx4 v[28:29], v[24:27], off
	s_cbranch_scc0 .LBB0_1879
; __device__ __forceinline__ void rwkv_post_ph(const int WID_, const float* __restrict__ Y, const float* __restrict__ RK, const bf16* __restrict__ proj, const float* __restrict__ mu, const bf16* __restrict__ G, ...
;     ...
;     for (int g = g_lo; g < g_hi; ++g) { const int m0 = g * 16 + tk;
;         float4 ya[2], yb[2]; uint4 vv[2], pv[2], gg[2]; float rk[2];
; #pragma unroll
;         for (int u = 0; u < 2; ++u) { const int m = m0 + 8 * u;
;             ya[u] = *(const float4*)(Y + (size_t)m * 512 + ch0); yb[u] = *(const float4*)(Y + (size_t)m * 512 + ch0 + 4);
;             vv[u] = *(const uint4*)(proj + (size_t)m * DSHIFT + 1024 + ch0);
;             pv[u] = (m & (S - 1)) ? *(const uint4*)(proj + (size_t)(m - 1) * DSHIFT + 1024 + ch0) : make_uint4(0, 0, 0, 0);
;             gg[u] = *(const uint4*)(G + (size_t)m * 512 + ch0); rk[u] = RK[(size_t)m * 8 + head]; }
.LBB0_1874:
	s_ashr_i32 s1, s0, 31
	s_lshl_b64 s[36:37], s[0:1], 11
	v_lshl_add_u64 v[24:25], v[60:61], 0, s[36:37]
	global_load_dwordx4 v[32:35], v[24:25], off offset:16 nt
	global_load_dwordx4 v[28:31], v[24:25], off nt
	v_mad_i64_i32 v[24:25], s[22:23], s0, v71, v[68:69]
	global_load_dwordx4 v[48:51], v[24:25], off offset:2048 nt
	s_and_b32 s22, s0, 0x1fff
	s_cmp_eq_u32 s22, 0
	s_cbranch_scc1 .LBB0_1876
	s_add_i32 s22, s0, -1
	v_mad_i64_i32 v[24:25], s[22:23], s22, v71, v[68:69]
	global_load_dwordx4 v[52:55], v[24:25], off offset:2048 nt
	s_branch .LBB0_1877

; __device__ __forceinline__ void rwkv_post_ph(const int WID_, const float* __restrict__ Y, const float* __restrict__ RK, const bf16* __restrict__ proj, const float* __restrict__ mu, const bf16* __restrict__ G, ...
;     ...
;         for (int u = 0; u < 2; ++u) { const int m = m0 + 8 * u;
;             ya[u] = *(const float4*)(Y + (size_t)m * 512 + ch0); yb[u] = *(const float4*)(Y + (size_t)m * 512 + ch0 + 4);
;             vv[u] = *(const uint4*)(proj + (size_t)m * DSHIFT + 1024 + ch0);
;             pv[u] = (m & (S - 1)) ? *(const uint4*)(proj + (size_t)(m - 1) * DSHIFT + 1024 + ch0) : make_uint4(0, 0, 0, 0);
;             gg[u] = *(const uint4*)(G + (size_t)m * 512 + ch0); rk[u] = RK[(size_t)m * 8 + head]; }
.LBB0_1877:
	s_lshl_b64 s[22:23], s[0:1], 9
	s_add_i32 s38, s0, 8
	v_lshl_add_u64 v[24:25], s[22:23], 1, v[62:63]
	s_lshl_b64 s[22:23], s[0:1], 5
	s_ashr_i32 s39, s38, 31
	v_lshl_add_u64 v[26:27], v[64:65], 0, s[22:23]
	s_lshl_b64 s[22:23], s[38:39], 11
	global_load_dwordx4 v[56:59], v[24:25], off nt
	global_load_dword v72, v[26:27], off
	v_lshl_add_u64 v[24:25], v[60:61], 0, s[22:23]
	global_load_dwordx4 v[40:43], v[24:25], off offset:16 nt
	global_load_dwordx4 v[36:39], v[24:25], off nt
	v_mad_i64_i32 v[24:25], s[34:35], s38, v71, v[68:69]
	global_load_dwordx4 v[44:47], v[24:25], off offset:2048 nt
	s_lshl_b64 s[40:41], s[38:39], 9
	s_and_b32 s1, s38, 0x1fff
	s_cmp_eq_u32 s1, 0
	s_cbranch_scc0 .LBB0_1872
	v_mov_b32_e32 v24, 0
	v_mov_b32_e32 v25, 0
	v_mov_b32_e32 v26, 0
	v_mov_b32_e32 v27, 0
	s_branch .LBB0_1873

; __device__ __forceinline__ int lane_id() { int l; asm volatile("v_mbcnt_lo_u32_b32 %0, -1, 0\n\tv_mbcnt_hi_u32_b32 %0, -1, %0" : "=v"(l)); return l; }
; __device__ __forceinline__ void rwkv_post_ph(const int WID_, const float* __restrict__ Y, const float* __restrict__ RK, const bf16* __restrict__ proj, const float* __restrict__ mu, const bf16* __restrict__ G, ...
;     const int lane = lane_id(), tk = WID_, grp = lane, ch0 = grp * 8, head = grp >> 3;
;     const float4 mv0 = *(const float4*)(mu + 1024 + ch0), mv1 = *(const float4*)(mu + 1024 + ch0 + 4), lw0 = *(const float4*)(lnw + ch0), lw1 = *(const float4*)(lnw + ch0 + 4), lb0 = *(const float4*)(lnb + ch0), lb1 = *(const float4*)(lnb + ch0 + 4);
;     const float muv[8] = {mv0.x, mv0.y, mv0.z, mv0.w, mv1.x, mv1.y, mv1.z, mv1.w}, lw_[8] = {lw0.x, lw0.y, lw0.z, lw0.w, lw1.x, lw1.y, lw1.z, lw1.w}, lb_[8] = {lb0.x, lb0.y, lb0.z, lb0.w, lb1.x, lb1.y, lb1.z, lb1.w};
;     const int g_lo = (GB * (M / 16)) / GN, g_hi = ((GB + 1) * (M / 16)) / GN;
;     for (int g = g_lo; g < g_hi; ++g) { const int m0 = g * 16 + tk;
;         float4 ya[2], yb[2]; uint4 vv[2], pv[2], gg[2]; float rk[2];
; #pragma unroll
;         for (int u = 0; u < 2; ++u) { const int m = m0 + 8 * u;
;             ya[u] = *(const float4*)(Y + (size_t)m * 512 + ch0); yb[u] = *(const float4*)(Y + (size_t)m * 512 + ch0 + 4);
;             vv[u] = *(const uint4*)(proj + (size_t)m * DSHIFT + 1024 + ch0);
;             pv[u] = (m & (S - 1)) ? *(const uint4*)(proj + (size_t)(m - 1) * DSHIFT + 1024 + ch0) : make_uint4(0, 0, 0, 0);
;             gg[u] = *(const uint4*)(G + (size_t)m * 512 + ch0); rk[u] = RK[(size_t)m * 8 + head]; }
.LBB0_1935:
	s_andn2_b64 vcc, exec, s[18:19]
	s_cbranch_vccnz .LBB0_1946
	s_lshl_b32 s1, s87, 12
	s_bfe_i32 s0, s87, 0x10013
	v_readlane_b32 s9, v243, 45
	s_xor_b32 s2, s0, s9
	s_abs_i32 s0, s1
	v_readlane_b32 s8, v242, 32
	s_mul_hi_u32 s3, s0, s8
	v_readlane_b32 s14, v242, 33
	s_mul_i32 s6, s3, s14
	s_sub_i32 s0, s0, s6
	s_add_i32 s6, s3, 1
	s_sub_i32 s7, s0, s14
	s_cmp_ge_u32 s0, s14
	s_cselect_b32 s3, s6, s3
	s_cselect_b32 s0, s7, s0
	s_add_i32 s6, s3, 1
	s_cmp_ge_u32 s0, s14
	s_cselect_b32 s0, s6, s3
	s_addk_i32 s1, 0x1000
	s_ashr_i32 s6, s1, 31
	s_abs_i32 s1, s1
	s_mul_hi_u32 s7, s1, s8
	s_mul_i32 s8, s7, s14
	s_xor_b32 s3, s0, s2
	s_sub_i32 s1, s1, s8
	s_sub_i32 s0, s3, s2
	s_xor_b32 s6, s6, s9
	s_add_i32 s8, s7, 1
	s_sub_i32 s9, s1, s14
	s_cmp_ge_u32 s1, s14
	s_cselect_b32 s7, s8, s7
	s_cselect_b32 s1, s9, s1
	s_add_i32 s8, s7, 1
	s_cmp_ge_u32 s1, s14
	s_cselect_b32 s1, s8, s7
	s_xor_b32 s1, s1, s6
	s_sub_i32 s1, s1, s6
	s_cmp_ge_i32 s0, s1
	v_mbcnt_lo_u32_b32 v24, -1, 0
	v_mbcnt_hi_u32_b32 v24, -1, v24
	s_cbranch_scc1 .LBB0_1946
	v_lshlrev_b32_e32 v26, 3, v24
	v_ashrrev_i32_e32 v27, 31, v26
	v_lshlrev_b64 v[28:29], 2, v[26:27]
	v_lshl_add_u64 v[0:1], s[64:65], 0, v[28:29]
	v_readlane_b32 s60, v243, 6
	s_mov_b64 s[6:7], 0x1000
	v_readlane_b32 s70, v243, 16
	v_readlane_b32 s71, v243, 17
	v_readlane_b32 s72, v243, 18
	v_readlane_b32 s73, v243, 19
	v_lshl_add_u64 v[4:5], v[0:1], 0, s[6:7]
	s_mov_b64 s[14:15], s[70:71]
	s_mov_b64 s[16:17], s[72:73]
	v_add_co_u32_e32 v0, vcc, 0x1000, v0
	v_lshl_add_u64 v[12:13], s[14:15], 0, v[28:29]
	v_lshl_add_u64 v[20:21], s[16:17], 0, v[28:29]
	v_addc_co_u32_e32 v1, vcc, 0, v1, vcc
	global_load_dwordx4 v[0:3], v[0:1], off nt
	s_nop 0
	global_load_dwordx4 v[4:7], v[4:5], off offset:16 nt
	s_nop 0
	global_load_dwordx4 v[8:11], v[12:13], off offset:16 nt
	s_nop 0
	global_load_dwordx4 v[12:15], v[12:13], off nt
	s_nop 0
	global_load_dwordx4 v[16:19], v[20:21], off offset:16 nt
	s_nop 0
	global_load_dwordx4 v[20:23], v[20:21], off nt
	v_lshlrev_b64 v[26:27], 1, v[26:27]
	v_ashrrev_i32_e32 v24, 3, v24
	v_lshl_add_u64 v[62:63], s[4:5], 0, v[26:27]
	s_lshl_b32 s3, s3, 4
	v_readlane_b32 s4, v243, 44
	v_ashrrev_i32_e32 v25, 31, v24
	s_add_i32 s3, s4, s3
	s_lshl_b32 s2, s2, 4
	v_lshl_add_u64 v[60:61], s[12:13], 0, v[28:29]
	v_lshl_add_u64 v[64:65], v[24:25], 2, s[10:11]
	v_lshl_add_u64 v[66:67], s[26:27], 0, v[26:27]
	v_lshl_add_u64 v[68:69], s[92:93], 0, v[26:27]
	s_sub_i32 s2, s3, s2
	s_mov_b32 s4, 0x3c800000
	s_mov_b32 s5, 0x800000
	v_mov_b32_e32 v71, 0xe00
	v_mov_b32_e32 v70, 0x3a27c5ac
	v_readlane_b32 s61, v243, 7
	v_readlane_b32 s62, v243, 8
	v_readlane_b32 s63, v243, 9
	v_readlane_b32 s64, v243, 10
	v_readlane_b32 s65, v243, 11
	v_readlane_b32 s66, v243, 12
	v_readlane_b32 s67, v243, 13
	v_readlane_b32 s68, v243, 14
	v_readlane_b32 s69, v243, 15
	v_readlane_b32 s74, v243, 20
	v_readlane_b32 s75, v243, 21
	s_branch .LBB0_1940
.LBB0_1938:
	s_add_i32 s3, s2, 7
	v_mad_i64_i32 v[24:25], s[14:15], s3, v71, v[68:69]
	global_load_dwordx4 v[24:27], v[24:25], off offset:2048 nt
.LBB0_1939:
	s_lshl_b64 s[10:11], s[10:11], 5
	v_lshl_add_u64 v[74:75], s[12:13], 1, v[62:63]
	v_lshl_add_u64 v[96:97], v[64:65], 0, s[10:11]
	global_load_dwordx4 v[74:77], v[74:75], off nt
	s_waitcnt vmcnt(0)
	v_lshlrev_b32_e32 v94, 16, v46
	v_and_b32_e32 v95, 0xffff0000, v46
	global_load_dword v46, v[96:97], off
	v_add_f32_e32 v73, 0, v28
	v_lshlrev_b32_e32 v84, 16, v50
	v_lshlrev_b32_e32 v86, 16, v54
	v_and_b32_e32 v85, 0xffff0000, v50
	v_and_b32_e32 v87, 0xffff0000, v54
	v_lshlrev_b32_e32 v50, 16, v51
	v_lshlrev_b32_e32 v54, 16, v55
	v_and_b32_e32 v51, 0xffff0000, v51
	v_and_b32_e32 v55, 0xffff0000, v55
	v_add_f32_e32 v98, 0, v36
	v_add_f32_e32 v73, v73, v29
	v_pk_add_f32 v[54:55], v[54:55], v[50:51] neg_lo:[0,1] neg_hi:[0,1]
	v_add_f32_e32 v98, v98, v37
	v_add_f32_e32 v73, v73, v30
	v_pk_fma_f32 v[50:51], v[6:7], v[54:55], v[50:51]
	v_add_f32_e32 v54, v98, v38
	v_add_f32_e32 v55, v73, v31
	v_add_f32_e32 v54, v54, v39
	v_add_f32_e32 v55, v55, v32
	v_add_f32_e32 v54, v54, v40
	v_add_f32_e32 v55, v55, v33
	v_add_f32_e32 v54, v54, v41
	v_add_f32_e32 v55, v55, v34
	v_add_f32_e32 v54, v54, v42
	v_add_f32_e32 v55, v55, v35
	v_add_f32_e32 v54, v54, v43
	v_lshlrev_b32_e32 v78, 16, v48
	v_add_f32_dpp v55, v55, v55 quad_perm:[1,0,3,2] row_mask:0xf bank_mask:0xf bound_ctrl:1
	v_add_f32_dpp v54, v54, v54 quad_perm:[1,0,3,2] row_mask:0xf bank_mask:0xf bound_ctrl:1
	v_lshlrev_b32_e32 v80, 16, v52
	v_and_b32_e32 v79, 0xffff0000, v48
	v_and_b32_e32 v81, 0xffff0000, v52
	v_lshlrev_b32_e32 v48, 16, v49
	v_lshlrev_b32_e32 v52, 16, v53
	v_and_b32_e32 v49, 0xffff0000, v49
	v_and_b32_e32 v53, 0xffff0000, v53
	v_add_f32_dpp v55, v55, v55 quad_perm:[2,3,0,1] row_mask:0xf bank_mask:0xf bound_ctrl:1
	v_add_f32_dpp v54, v54, v54 quad_perm:[2,3,0,1] row_mask:0xf bank_mask:0xf bound_ctrl:1
	v_pk_add_f32 v[52:53], v[52:53], v[48:49] neg_lo:[0,1] neg_hi:[0,1]
	v_pk_add_f32 v[80:81], v[80:81], v[78:79] neg_lo:[0,1] neg_hi:[0,1]
	v_add_f32_dpp v55, v55, v55 row_half_mirror row_mask:0xf bank_mask:0xf bound_ctrl:1
	v_add_f32_dpp v73, v54, v54 row_half_mirror row_mask:0xf bank_mask:0xf bound_ctrl:1
	v_pk_fma_f32 v[48:49], v[2:3], v[52:53], v[48:49]
	v_pk_fma_f32 v[52:53], v[0:1], v[80:81], v[78:79]
	v_mul_f32_e32 v54, 0x3c800000, v55
	v_mul_f32_e32 v78, 0x3c800000, v73
	v_lshlrev_b32_e32 v92, 16, v44
	v_and_b32_e32 v93, 0xffff0000, v44
	v_lshlrev_b32_e32 v44, 16, v45
	v_and_b32_e32 v45, 0xffff0000, v45
	v_pk_add_f32 v[28:29], v[28:29], v[54:55] op_sel_hi:[1,0] neg_lo:[0,1] neg_hi:[0,1]
	v_lshlrev_b32_e32 v108, 16, v26
	v_and_b32_e32 v109, 0xffff0000, v26
; __device__ __forceinline__ unsigned pk2(float lo, float hi) { const f32x2h v = {lo, hi}; const bf16x2h b = __builtin_convertvector(v, bf16x2h); return __builtin_bit_cast(unsigned, b); }
; template <int CTRL> __device__ __forceinline__ float dpp16(float x) { return __builtin_bit_cast(float, __builtin_amdgcn_update_dpp(0, __builtin_bit_cast(int, x), CTRL, 0xf, 0xf, true)); }
; __device__ __forceinline__ void rwkv_post_ph(const int WID_, const float* __restrict__ Y, const float* __restrict__ RK, const bf16* __restrict__ proj, const float* __restrict__ mu, const bf16* __restrict__ G, ...
;     ...
; #pragma unroll
;         for (int u = 0; u < 2; ++u) {
;             const float y[8] = {ya[u].x, ya[u].y, ya[u].z, ya[u].w, yb[u].x, yb[u].y, yb[u].z, yb[u].w};
;             float s = 0.f;
; #pragma unroll
;             for (int e = 0; e < 8; ++e) s += y[e];
;             s += dpp16<0xB1>(s); s += dpp16<0x4E>(s); s += dpp16<0x141>(s);
;             const float mean = s * (1.f / 64.f); float q = 0.f;
; #pragma unroll
;             for (int e = 0; e < 8; ++e) { const float d = y[e] - mean; q += d * d; }
;             q += dpp16<0xB1>(q); q += dpp16<0x4E>(q); q += dpp16<0x141>(q);
;             const float rstd = rsqrtf(q * (1.f / 64.f) + 64e-5f);
;             const unsigned wv_[4] = {vv[u].x, vv[u].y, vv[u].z, vv[u].w}, wp_[4] = {pv[u].x, pv[u].y, pv[u].z, pv[u].w}, wg_[4] = {gg[u].x, gg[u].y, gg[u].z, gg[u].w};
;             float o[8];
; #pragma unroll
;             for (int e = 0; e < 8; ++e) { const int w_ = e >> 1; const bool hi = e & 1;
;                 auto ex = [&](unsigned x) { return hi ? __builtin_bit_cast(float, x & 0xffff0000u) : __builtin_bit_cast(float, x << 16); };
;                 float v = ex(wv_[w_]); v += (ex(wp_[w_]) - v) * muv[e];
;                 o[e] = ((y[e] - mean) * rstd * lw_[e] + lb_[e] + rk[u] * v) * ex(wg_[w_]); }
;             *(uint4*)(ymix + (size_t)(m0 + 8 * u) * D + ch0) = make_uint4(pk2(o[0], o[1]), pk2(o[2], o[3]), pk2(o[4], o[5]), pk2(o[6], o[7]));
;         }
	v_lshlrev_b32_e32 v110, 16, v25
	v_and_b32_e32 v111, 0xffff0000, v25
	v_pk_add_f32 v[36:37], v[36:37], v[78:79] op_sel_hi:[1,0] neg_lo:[0,1] neg_hi:[0,1]
	v_pk_add_f32 v[86:87], v[86:87], v[84:85] neg_lo:[0,1] neg_hi:[0,1]
	v_pk_add_f32 v[30:31], v[30:31], v[54:55] op_sel_hi:[1,0] neg_lo:[0,1] neg_hi:[0,1]
	v_pk_mul_f32 v[96:97], v[28:29], v[28:29]
	v_pk_add_f32 v[42:43], v[42:43], v[78:79] op_sel_hi:[1,0] neg_lo:[0,1] neg_hi:[0,1]
	v_pk_add_f32 v[40:41], v[40:41], v[78:79] op_sel_hi:[1,0] neg_lo:[0,1] neg_hi:[0,1]
	v_pk_add_f32 v[108:109], v[108:109], v[94:95] neg_lo:[0,1] neg_hi:[0,1]
	v_pk_add_f32 v[38:39], v[38:39], v[78:79] op_sel_hi:[1,0] neg_lo:[0,1] neg_hi:[0,1]
	v_pk_add_f32 v[110:111], v[110:111], v[44:45] neg_lo:[0,1] neg_hi:[0,1]
	v_pk_mul_f32 v[78:79], v[36:37], v[36:37]
	v_pk_fma_f32 v[84:85], v[4:5], v[86:87], v[84:85]
	v_pk_mul_f32 v[86:87], v[30:31], v[30:31]
	v_pk_fma_f32 v[94:95], v[4:5], v[108:109], v[94:95]
	v_pk_mul_f32 v[108:109], v[38:39], v[38:39]
	v_pk_fma_f32 v[44:45], v[2:3], v[110:111], v[44:45]
	v_mov_b32_e32 v110, v78
	v_mov_b32_e32 v111, v96
	v_mov_b32_e32 v96, v79
	v_pk_add_f32 v[32:33], v[32:33], v[54:55] op_sel_hi:[1,0] neg_lo:[0,1] neg_hi:[0,1]
	v_pk_add_f32 v[78:79], v[110:111], v[96:97]
	v_mov_b32_e32 v110, v108
	v_mov_b32_e32 v111, v86
	v_pk_mul_f32 v[80:81], v[32:33], v[32:33]
	v_pk_mul_f32 v[106:107], v[40:41], v[40:41]
	v_pk_add_f32 v[78:79], v[110:111], v[78:79]
	v_mov_b32_e32 v86, v109
	v_pk_add_f32 v[34:35], v[34:35], v[54:55] op_sel_hi:[1,0] neg_lo:[0,1] neg_hi:[0,1]
	v_pk_add_f32 v[78:79], v[86:87], v[78:79]
	v_mov_b32_e32 v86, v106
	v_mov_b32_e32 v87, v80
	v_pk_mul_f32 v[54:55], v[34:35], v[34:35]
	v_pk_mul_f32 v[104:105], v[42:43], v[42:43]
	v_pk_add_f32 v[78:79], v[86:87], v[78:79]
	v_mov_b32_e32 v80, v107
	v_pk_add_f32 v[78:79], v[80:81], v[78:79]
	v_mov_b32_e32 v80, v104
	v_mov_b32_e32 v81, v54
	v_pk_add_f32 v[78:79], v[80:81], v[78:79]
	v_mov_b32_e32 v54, v105
	v_pk_add_f32 v[54:55], v[54:55], v[78:79]
	v_lshlrev_b32_e32 v102, 16, v47
	v_and_b32_e32 v103, 0xffff0000, v47
	v_mov_b32_dpp v79, v55 quad_perm:[1,0,3,2] row_mask:0xf bank_mask:0xf bound_ctrl:1
	v_mov_b32_dpp v78, v54 quad_perm:[1,0,3,2] row_mask:0xf bank_mask:0xf bound_ctrl:1
	v_pk_add_f32 v[54:55], v[54:55], v[78:79]
	v_lshlrev_b32_e32 v82, 16, v56
	v_and_b32_e32 v83, 0xffff0000, v56
	v_mov_b32_dpp v79, v55 quad_perm:[2,3,0,1] row_mask:0xf bank_mask:0xf bound_ctrl:1
	v_mov_b32_dpp v78, v54 quad_perm:[2,3,0,1] row_mask:0xf bank_mask:0xf bound_ctrl:1
	v_pk_add_f32 v[54:55], v[54:55], v[78:79]
	v_lshlrev_b32_e32 v56, 16, v57
	v_and_b32_e32 v57, 0xffff0000, v57
	v_mov_b32_dpp v79, v55 row_half_mirror row_mask:0xf bank_mask:0xf bound_ctrl:1
	v_mov_b32_dpp v78, v54 row_half_mirror row_mask:0xf bank_mask:0xf bound_ctrl:1
	v_pk_add_f32 v[54:55], v[54:55], v[78:79]
	v_lshlrev_b32_e32 v88, 16, v58
	v_pk_fma_f32 v[54:55], v[54:55], s[4:5], v[70:71] op_sel_hi:[1,0,0]
	v_and_b32_e32 v89, 0xffff0000, v58
	v_mul_f32_e32 v25, 0x4b800000, v55
	v_cmp_gt_f32_e32 vcc, s5, v55
	v_lshlrev_b32_e32 v58, 16, v59
	v_and_b32_e32 v59, 0xffff0000, v59
	v_cndmask_b32_e32 v25, v55, v25, vcc
	v_rsq_f32_e32 v26, v25
	v_lshl_add_u64 v[90:91], v[66:67], 0, s[8:9]
	v_lshlrev_b32_e32 v96, 16, v24
	v_and_b32_e32 v97, 0xffff0000, v24
	v_mul_f32_e32 v47, 0x45800000, v26
	v_cndmask_b32_e32 v26, v26, v47, vcc
	v_pk_mul_f32 v[28:29], v[28:29], v[26:27] op_sel_hi:[1,0]
	v_pk_mul_f32 v[30:31], v[30:31], v[26:27] op_sel_hi:[1,0]
	v_pk_mul_f32 v[32:33], v[32:33], v[26:27] op_sel_hi:[1,0]
	v_pk_mul_f32 v[34:35], v[34:35], v[26:27] op_sel_hi:[1,0]
	v_mul_f32_e32 v26, 0x4b800000, v54
	v_cmp_gt_f32_e32 vcc, s5, v54
	v_pk_fma_f32 v[28:29], v[12:13], v[28:29], v[20:21]
	v_pk_fma_f32 v[30:31], v[14:15], v[30:31], v[22:23]
	v_cndmask_b32_e32 v26, v54, v26, vcc
	v_pk_fma_f32 v[32:33], v[8:9], v[32:33], v[16:17]
	v_pk_fma_f32 v[34:35], v[10:11], v[34:35], v[18:19]
	v_rsq_f32_e32 v26, v26
	v_pk_fma_f32 v[28:29], v[52:53], v[72:73], v[28:29] op_sel_hi:[1,0,1]
	v_pk_fma_f32 v[30:31], v[48:49], v[72:73], v[30:31] op_sel_hi:[1,0,1]
	v_pk_fma_f32 v[32:33], v[84:85], v[72:73], v[32:33] op_sel_hi:[1,0,1]
	v_pk_fma_f32 v[34:35], v[50:51], v[72:73], v[34:35] op_sel_hi:[1,0,1]
	v_pk_mul_f32 v[28:29], v[28:29], v[82:83]
	v_pk_mul_f32 v[30:31], v[30:31], v[56:57]
	v_pk_mul_f32 v[32:33], v[32:33], v[88:89]
	v_pk_mul_f32 v[34:35], v[34:35], v[58:59]
	v_cvt_pk_bf16_f32 v28, v28, v29
	v_cvt_pk_bf16_f32 v29, v30, v31
	v_cvt_pk_bf16_f32 v30, v32, v33
	v_cvt_pk_bf16_f32 v31, v34, v35
	global_store_dwordx4 v[90:91], v[28:31], off
	v_pk_add_f32 v[24:25], v[96:97], v[92:93] neg_lo:[0,1] neg_hi:[0,1]
	v_lshlrev_b32_e32 v32, 16, v27
	v_mul_f32_e32 v28, 0x45800000, v26
	v_cndmask_b32_e32 v26, v26, v28, vcc
	v_pk_mul_f32 v[28:29], v[36:37], v[26:27] op_sel_hi:[1,0]
	v_pk_fma_f32 v[24:25], v[0:1], v[24:25], v[92:93]
	v_pk_fma_f32 v[28:29], v[12:13], v[28:29], v[20:21]
	v_and_b32_e32 v33, 0xffff0000, v27
	s_waitcnt vmcnt(1)
	v_pk_fma_f32 v[24:25], v[24:25], v[46:47], v[28:29] op_sel_hi:[1,0,1]
	v_pk_mul_f32 v[28:29], v[38:39], v[26:27] op_sel_hi:[1,0]
	v_pk_mul_f32 v[30:31], v[40:41], v[26:27] op_sel_hi:[1,0]
	v_pk_add_f32 v[32:33], v[32:33], v[102:103] neg_lo:[0,1] neg_hi:[0,1]
	v_pk_mul_f32 v[26:27], v[42:43], v[26:27] op_sel_hi:[1,0]
	v_pk_fma_f32 v[28:29], v[14:15], v[28:29], v[22:23]
	v_pk_fma_f32 v[30:31], v[8:9], v[30:31], v[16:17]
	v_pk_fma_f32 v[32:33], v[6:7], v[32:33], v[102:103]
	v_pk_fma_f32 v[26:27], v[10:11], v[26:27], v[18:19]
	v_lshlrev_b32_e32 v98, 16, v74
	v_and_b32_e32 v99, 0xffff0000, v74
	v_lshlrev_b32_e32 v74, 16, v75
	v_and_b32_e32 v75, 0xffff0000, v75
	v_lshlrev_b32_e32 v100, 16, v76
	v_and_b32_e32 v101, 0xffff0000, v76
	v_lshlrev_b32_e32 v76, 16, v77
	v_and_b32_e32 v77, 0xffff0000, v77
	v_pk_fma_f32 v[28:29], v[44:45], v[46:47], v[28:29] op_sel_hi:[1,0,1]
	v_pk_fma_f32 v[30:31], v[94:95], v[46:47], v[30:31] op_sel_hi:[1,0,1]
	v_pk_fma_f32 v[26:27], v[32:33], v[46:47], v[26:27] op_sel_hi:[1,0,1]
	v_pk_mul_f32 v[24:25], v[24:25], v[98:99]
	v_pk_mul_f32 v[28:29], v[28:29], v[74:75]
	v_pk_mul_f32 v[30:31], v[30:31], v[100:101]
	v_pk_mul_f32 v[32:33], v[26:27], v[76:77]
	s_add_i32 s0, s0, 1
	s_add_i32 s2, s2, 16
	v_cvt_pk_bf16_f32 v24, v24, v25
	v_cvt_pk_bf16_f32 v25, v28, v29
	v_cvt_pk_bf16_f32 v26, v30, v31
	v_cvt_pk_bf16_f32 v27, v32, v33
	v_lshl_add_u64 v[28:29], v[66:67], 0, s[6:7]
	s_cmp_lt_i32 s0, s1
	global_store_dwordx4 v[28:29], v[24:27], off
	s_cbranch_scc0 .LBB0_1945
.LBB0_1940:
	s_ashr_i32 s3, s2, 31
	s_lshl_b64 s[8:9], s[2:3], 11
	v_lshl_add_u64 v[24:25], v[60:61], 0, s[8:9]
	global_load_dwordx4 v[32:35], v[24:25], off offset:16 nt
	global_load_dwordx4 v[28:31], v[24:25], off nt
	v_mad_i64_i32 v[24:25], s[6:7], s2, v71, v[68:69]
	global_load_dwordx4 v[48:51], v[24:25], off offset:2048 nt
	s_and_b32 s6, s2, 0x1fff
	s_cmp_eq_u32 s6, 0
	s_cbranch_scc1 .LBB0_1942
	s_add_i32 s6, s2, -1
	v_mad_i64_i32 v[24:25], s[6:7], s6, v71, v[68:69]
	global_load_dwordx4 v[52:55], v[24:25], off offset:2048 nt
	s_branch .LBB0_1943

; __device__ __forceinline__ void rwkv_post_ph(const int WID_, const float* __restrict__ Y, const float* __restrict__ RK, const bf16* __restrict__ proj, const float* __restrict__ mu, const bf16* __restrict__ G, ...
;     ...
;         for (int u = 0; u < 2; ++u) { const int m = m0 + 8 * u;
;             ya[u] = *(const float4*)(Y + (size_t)m * 512 + ch0); yb[u] = *(const float4*)(Y + (size_t)m * 512 + ch0 + 4);
;             vv[u] = *(const uint4*)(proj + (size_t)m * DSHIFT + 1024 + ch0);
;             pv[u] = (m & (S - 1)) ? *(const uint4*)(proj + (size_t)(m - 1) * DSHIFT + 1024 + ch0) : make_uint4(0, 0, 0, 0);
;             gg[u] = *(const uint4*)(G + (size_t)m * 512 + ch0); rk[u] = RK[(size_t)m * 8 + head]; }
.LBB0_1943:
	s_lshl_b64 s[6:7], s[2:3], 9
	s_add_i32 s10, s2, 8
	v_lshl_add_u64 v[24:25], s[6:7], 1, v[62:63]
	s_lshl_b64 s[6:7], s[2:3], 5
	s_ashr_i32 s11, s10, 31
	v_lshl_add_u64 v[26:27], v[64:65], 0, s[6:7]
	s_lshl_b64 s[6:7], s[10:11], 11
	global_load_dwordx4 v[56:59], v[24:25], off nt
	global_load_dword v72, v[26:27], off
	v_lshl_add_u64 v[24:25], v[60:61], 0, s[6:7]
	global_load_dwordx4 v[40:43], v[24:25], off offset:16 nt
	global_load_dwordx4 v[36:39], v[24:25], off nt
	v_mad_i64_i32 v[24:25], s[12:13], s10, v71, v[68:69]
	global_load_dwordx4 v[44:47], v[24:25], off offset:2048 nt
	s_lshl_b64 s[12:13], s[10:11], 9
	s_and_b32 s3, s10, 0x1fff
	s_cmp_eq_u32 s3, 0
	s_cbranch_scc0 .LBB0_1938
	v_mov_b32_e32 v24, 0
	v_mov_b32_e32 v25, 0
	v_mov_b32_e32 v26, 0
	v_mov_b32_e32 v27, 0
	s_branch .LBB0_1939
